# baseline (speedup 1.0000x reference)
_Z2kBPKfPKDv4_jPKDF16_S0_S0_S0_Pf:
	v_lshrrev_b32_e32 v11, 7, v0
	s_load_dwordx8 s[4:11], s[0:1], 0x0
	v_lshl_or_b32 v2, s2, 2, v11
	s_mov_b32 s2, 0x4ec4ec4f
	v_mul_hi_i32 v1, v2, s2
	v_lshrrev_b32_e32 v3, 31, v1
	v_ashrrev_i32_e32 v1, 2, v1
	v_add_u32_e32 v1, v1, v3
	v_and_b32_e32 v108, 15, v0
	v_mad_u64_u32 v[4:5], s[2:3], v1, -13, v[2:3]
	v_lshlrev_b32_e32 v102, 4, v0
	v_mov_b32_e32 v103, 0
	v_lshl_or_b32 v10, v4, 4, v108
	s_waitcnt lgkmcnt(0)
	v_readfirstlane_b32 s12, v0
	v_and_b32_e32 v4, 63, v0
	v_lshlrev_b32_e32 v4, 4, v4
	s_lshl_b32 s12, s12, 4
	s_add_u32 s14, s8, s12
	s_addc_u32 s15, s9, 0
	s_mov_b32 m0, s12
	s_nop 0
	global_load_lds_dwordx4 v4, s[14:15]
	s_add_u32 m0, m0, 0x2000
	s_add_u32 s14, s14, 0x2000
	s_addc_u32 s15, s15, 0
	global_load_lds_dwordx4 v4, s[14:15]
	s_add_u32 m0, m0, 0x2000
	s_add_u32 s14, s14, 0x2000
	s_addc_u32 s15, s15, 0
	global_load_lds_dwordx4 v4, s[14:15]
	s_add_u32 m0, m0, 0x2000
	s_add_u32 s14, s14, 0x2000
	s_addc_u32 s15, s15, 0
	global_load_lds_dwordx4 v4, s[14:15]
	s_add_u32 m0, m0, 0x2000
	s_add_u32 s14, s14, 0x2000
	s_addc_u32 s15, s15, 0
	global_load_lds_dwordx4 v4, s[14:15]
	s_add_u32 m0, m0, 0x2000
	s_add_u32 s14, s14, 0x2000
	s_addc_u32 s15, s15, 0
	global_load_lds_dwordx4 v4, s[14:15]
	s_add_u32 m0, m0, 0x2000
	s_add_u32 s14, s14, 0x2000
	s_addc_u32 s15, s15, 0
	global_load_lds_dwordx4 v4, s[14:15]
	s_add_u32 m0, m0, 0x2000
	s_add_u32 s14, s14, 0x2000
	s_addc_u32 s15, s15, 0
	global_load_lds_dwordx4 v4, s[14:15]
	s_movk_i32 s2, 0xc8
	v_mov_b32_e32 v3, 0xc7
	v_cmp_gt_i32_e32 vcc, s2, v10
	s_movk_i32 s2, 0x320
	v_cndmask_b32_e32 v4, v3, v10, vcc
	v_mad_u64_u32 v[4:5], s[2:3], v1, s2, v[4:5]
	v_and_b32_e32 v6, 48, v0
	v_mov_b32_e32 v7, v103
	v_ashrrev_i32_e32 v5, 31, v4
	v_lshl_add_u64 v[8:9], s[4:5], 0, v[6:7]
	v_lshlrev_b64 v[12:13], 6, v[4:5]
	v_lshl_add_u64 v[12:13], v[8:9], 0, v[12:13]
	global_load_dwordx4 v[46:49], v[12:13], off
	v_add_u32_e32 v12, 0xc8, v4
	v_ashrrev_i32_e32 v13, 31, v12
	v_lshlrev_b64 v[12:13], 6, v[12:13]
	v_lshl_add_u64 v[12:13], v[8:9], 0, v[12:13]
	global_load_dwordx4 v[50:53], v[12:13], off
	v_add_u32_e32 v12, 0x190, v4
	v_ashrrev_i32_e32 v13, 31, v12
	v_lshlrev_b64 v[12:13], 6, v[12:13]
	v_lshl_add_u64 v[12:13], v[8:9], 0, v[12:13]
	global_load_dwordx4 v[54:57], v[12:13], off
	v_add_u32_e32 v4, 0x258, v4
	v_ashrrev_i32_e32 v5, 31, v4
	v_lshlrev_b64 v[4:5], 6, v[4:5]
	v_lshl_add_u64 v[4:5], v[8:9], 0, v[4:5]
	global_load_dwordx4 v[58:61], v[4:5], off
	v_and_b32_e32 v13, 63, v0
	v_lshl_or_b32 v2, v2, 8, v13
	v_ashrrev_i32_e32 v3, 31, v2
	v_lshl_add_u64 v[2:3], v[2:3], 4, s[6:7]
	global_load_dwordx4 v[62:65], v[2:3], off
	global_load_dwordx4 v[66:69], v[2:3], off offset:1024
	global_load_dwordx4 v[70:73], v[2:3], off offset:2048
	global_load_dwordx4 v[74:77], v[2:3], off offset:3072
	s_load_dwordx4 s[4:7], s[0:1], 0x20
	v_bfe_u32 v12, v0, 6, 1
	v_lshl_add_u64 v[2:3], s[10:11], 0, v[6:7]
	v_and_b32_e32 v0, 64, v0
	v_cmp_gt_u32_e64 s[2:3], 16, v13
	s_waitcnt lgkmcnt(0)
	v_lshl_add_u64 v[4:5], s[4:5], 0, v[6:7]
	v_lshlrev_b32_e32 v6, 8, v12
	v_lshl_add_u64 v[104:105], v[2:3], 0, v[6:7]
	v_lshl_add_u64 v[106:107], v[4:5], 0, v[6:7]
	global_load_dwordx4 v[78:81], v[104:105], off
	global_load_dwordx4 v[82:85], v[104:105], off offset:64
	global_load_dwordx4 v[86:89], v[106:107], off
	global_load_dwordx4 v[90:93], v[106:107], off offset:64
	global_load_dwordx4 v[94:97], v[104:105], off offset:128
	global_load_dwordx4 v[6:9], v[104:105], off offset:192
	global_load_dwordx4 v[98:101], v[106:107], off offset:128
	global_load_dwordx4 v[2:5], v[106:107], off offset:192
	s_load_dword s6, s[6:7], 0x0
	s_waitcnt vmcnt(16)
	v_lshlrev_b32_e32 v14, 15, v12
	v_lshl_or_b32 v38, v13, 4, v14
	s_waitcnt lgkmcnt(0)
	s_barrier
	ds_read_b128 v[14:17], v38
	ds_read_b128 v[18:21], v38 offset:1024
	s_waitcnt vmcnt(15) lgkmcnt(1)
	v_mfma_f32_16x16x32_f16 v[14:17], v[14:17], v[46:49], 0
	ds_read_b128 v[22:25], v38 offset:2048
	ds_read_b128 v[26:29], v38 offset:10240
	ds_read_b128 v[30:33], v38 offset:18432
	s_waitcnt vmcnt(14) lgkmcnt(3)
	v_mfma_f32_16x16x32_f16 v[14:17], v[18:21], v[50:53], v[14:17]
	ds_read_b128 v[18:21], v38 offset:3072
	ds_read_b128 v[34:37], v38 offset:26624
	v_cmp_ne_u32_e64 s[4:5], 0, v0
	s_waitcnt vmcnt(13) lgkmcnt(4)
	v_mfma_f32_16x16x32_f16 v[14:17], v[22:25], v[54:57], v[14:17]
	ds_read_b128 v[22:25], v38 offset:4096
	s_and_b64 s[8:9], s[4:5], s[2:3]
	v_lshlrev_b32_e32 v0, 2, v108
	s_waitcnt vmcnt(12) lgkmcnt(2)
	v_mfma_f32_16x16x32_f16 v[14:17], v[18:21], v[58:61], v[14:17]
	ds_read_b128 v[18:21], v38 offset:5120
	s_waitcnt vmcnt(11) lgkmcnt(1)
	v_mfma_f32_16x16x32_f16 v[14:17], v[22:25], v[62:65], v[14:17]
	ds_read_b128 v[22:25], v38 offset:6144
	s_waitcnt vmcnt(10) lgkmcnt(1)
	v_mfma_f32_16x16x32_f16 v[14:17], v[18:21], v[66:69], v[14:17]
	ds_read_b128 v[18:21], v38 offset:7168
	s_waitcnt vmcnt(9) lgkmcnt(1)
	v_mfma_f32_16x16x32_f16 v[14:17], v[22:25], v[70:73], v[14:17]
	ds_read_b128 v[22:25], v38 offset:8192
	s_waitcnt vmcnt(8) lgkmcnt(1)
	v_mfma_f32_16x16x32_f16 v[14:17], v[18:21], v[74:77], v[14:17]
	ds_read_b128 v[18:21], v38 offset:9216
	s_waitcnt lgkmcnt(1)
	v_mfma_f32_16x16x32_f16 v[22:25], v[22:25], v[46:49], 0
	s_waitcnt vmcnt(7)
	s_nop 3
	v_add_f32_e32 v14, v14, v78
	v_mul_f32_e32 v14, 0x4038aa3b, v14
	v_add_f32_e32 v15, v15, v79
	s_waitcnt lgkmcnt(0)
	v_mfma_f32_16x16x32_f16 v[18:21], v[18:21], v[50:53], v[22:25]
	v_exp_f32_e32 v14, v14
	v_mul_f32_e32 v15, 0x4038aa3b, v15
	s_nop 0
	ds_read_b128 v[22:25], v38 offset:11264
	v_mfma_f32_16x16x32_f16 v[18:21], v[26:29], v[54:57], v[18:21]
	ds_read_b128 v[26:29], v38 offset:12288
	v_add_f32_e32 v16, v16, v80
	v_exp_f32_e32 v15, v15
	s_waitcnt lgkmcnt(1)
	v_mfma_f32_16x16x32_f16 v[18:21], v[22:25], v[58:61], v[18:21]
	ds_read_b128 v[22:25], v38 offset:13312
	v_mul_f32_e32 v16, 0x4038aa3b, v16
	v_add_f32_e32 v17, v17, v81
	s_waitcnt lgkmcnt(1)
	v_mfma_f32_16x16x32_f16 v[18:21], v[26:29], v[62:65], v[18:21]
	ds_read_b128 v[26:29], v38 offset:14336
	v_exp_f32_e32 v16, v16
	v_mul_f32_e32 v17, 0x4038aa3b, v17
	s_waitcnt lgkmcnt(1)
	v_mfma_f32_16x16x32_f16 v[18:21], v[22:25], v[66:69], v[18:21]
	ds_read_b128 v[22:25], v38 offset:15360
	v_exp_f32_e32 v17, v17
	v_add_f32_e32 v14, 1.0, v14
	s_waitcnt lgkmcnt(1)
	v_mfma_f32_16x16x32_f16 v[18:21], v[26:29], v[70:73], v[18:21]
	ds_read_b128 v[26:29], v38 offset:16384
	v_rcp_f32_e32 v14, v14
	v_add_f32_e32 v15, 1.0, v15
	s_waitcnt lgkmcnt(1)
	v_mfma_f32_16x16x32_f16 v[18:21], v[22:25], v[74:77], v[18:21]
	ds_read_b128 v[22:25], v38 offset:17408
	v_rcp_f32_e32 v15, v15
	v_add_f32_e32 v16, 1.0, v16
	s_waitcnt lgkmcnt(1)
	v_mfma_f32_16x16x32_f16 v[26:29], v[26:29], v[46:49], 0
	v_rcp_f32_e32 v16, v16
	v_add_f32_e32 v17, 1.0, v17
	v_rcp_f32_e32 v17, v17
	s_waitcnt lgkmcnt(0)
	v_mfma_f32_16x16x32_f16 v[22:25], v[22:25], v[50:53], v[26:29]
	v_fma_f32 v14, v14, -2.0, 1.0
	s_nop 1
	ds_read_b128 v[26:29], v38 offset:19456
	s_waitcnt vmcnt(5)
	v_fma_f32 v14, v14, v86, 0
	v_mfma_f32_16x16x32_f16 v[22:25], v[30:33], v[54:57], v[22:25]
	ds_read_b128 v[30:33], v38 offset:20480
	v_fma_f32 v15, v15, -2.0, 1.0
	v_fmac_f32_e32 v14, v15, v87
	s_waitcnt lgkmcnt(1)
	v_mfma_f32_16x16x32_f16 v[22:25], v[26:29], v[58:61], v[22:25]
	ds_read_b128 v[26:29], v38 offset:21504
	v_fma_f32 v15, v16, -2.0, 1.0
	v_fmac_f32_e32 v14, v15, v88
	s_waitcnt lgkmcnt(1)
	v_mfma_f32_16x16x32_f16 v[22:25], v[30:33], v[62:65], v[22:25]
	ds_read_b128 v[30:33], v38 offset:22528
	v_fma_f32 v15, v17, -2.0, 1.0
	v_add_f32_e32 v16, v18, v82
	s_waitcnt lgkmcnt(1)
	v_mfma_f32_16x16x32_f16 v[22:25], v[26:29], v[66:69], v[22:25]
	ds_read_b128 v[26:29], v38 offset:23552
	v_add_f32_e32 v17, v19, v83
	v_mul_f32_e32 v16, 0x4038aa3b, v16
	s_waitcnt lgkmcnt(1)
	v_mfma_f32_16x16x32_f16 v[22:25], v[30:33], v[70:73], v[22:25]
	ds_read_b128 v[30:33], v38 offset:24576
	v_mul_f32_e32 v17, 0x4038aa3b, v17
	v_exp_f32_e32 v16, v16
	s_waitcnt lgkmcnt(1)
	v_mfma_f32_16x16x32_f16 v[22:25], v[26:29], v[74:77], v[22:25]
	ds_read_b128 v[26:29], v38 offset:25600
	v_exp_f32_e32 v17, v17
	v_fmac_f32_e32 v14, v15, v89
	s_waitcnt lgkmcnt(1)
	v_mfma_f32_16x16x32_f16 v[30:33], v[30:33], v[46:49], 0
	v_add_f32_e32 v15, 1.0, v16
	v_add_f32_e32 v16, 1.0, v17
	v_add_f32_e32 v17, v20, v84
	s_waitcnt lgkmcnt(0)
	v_mfma_f32_16x16x32_f16 v[26:29], v[26:29], v[50:53], v[30:33]
	v_rcp_f32_e32 v15, v15
	s_nop 1
	ds_read_b128 v[30:33], v38 offset:27648
	v_mul_f32_e32 v17, 0x4038aa3b, v17
	v_mfma_f32_16x16x32_f16 v[26:29], v[34:37], v[54:57], v[26:29]
	ds_read_b128 v[34:37], v38 offset:28672
	v_rcp_f32_e32 v16, v16
	v_exp_f32_e32 v17, v17
	s_waitcnt lgkmcnt(1)
	v_mfma_f32_16x16x32_f16 v[26:29], v[30:33], v[58:61], v[26:29]
	ds_read_b128 v[30:33], v38 offset:29696
	v_fma_f32 v15, v15, -2.0, 1.0
	s_waitcnt vmcnt(4)
	v_fmac_f32_e32 v14, v15, v90
	v_fma_f32 v15, v16, -2.0, 1.0
	v_add_f32_e32 v16, 1.0, v17
	v_add_f32_e32 v17, v21, v85
	s_waitcnt lgkmcnt(1)
	v_mfma_f32_16x16x32_f16 v[26:29], v[34:37], v[62:65], v[26:29]
	ds_read_b128 v[34:37], v38 offset:30720
	v_rcp_f32_e32 v16, v16
	v_mul_f32_e32 v17, 0x4038aa3b, v17
	v_exp_f32_e32 v17, v17
	s_waitcnt lgkmcnt(1)
	v_mfma_f32_16x16x32_f16 v[26:29], v[30:33], v[66:69], v[26:29]
	ds_read_b128 v[30:33], v38 offset:31744
	v_fmac_f32_e32 v14, v15, v91
	v_fma_f32 v15, v16, -2.0, 1.0
	s_waitcnt vmcnt(3)
	v_add_f32_e32 v16, v22, v94
	v_fmac_f32_e32 v14, v15, v92
	v_add_f32_e32 v15, 1.0, v17
	v_mul_f32_e32 v16, 0x4038aa3b, v16
	v_add_f32_e32 v17, v23, v95
	v_exp_f32_e32 v16, v16
	v_mul_f32_e32 v17, 0x4038aa3b, v17
	v_exp_f32_e32 v17, v17
	s_waitcnt lgkmcnt(1)
	v_mfma_f32_16x16x32_f16 v[26:29], v[34:37], v[70:73], v[26:29]
	v_rcp_f32_e32 v15, v15
	v_add_f32_e32 v16, 1.0, v16
	v_rcp_f32_e32 v16, v16
	v_add_f32_e32 v17, 1.0, v17
	v_rcp_f32_e32 v17, v17
	s_waitcnt lgkmcnt(0)
	v_mfma_f32_16x16x32_f16 v[26:29], v[30:33], v[74:77], v[26:29]
	v_fma_f32 v15, v15, -2.0, 1.0
	v_fmac_f32_e32 v14, v15, v93
	v_fma_f32 v15, v16, -2.0, 1.0
	v_add_f32_e32 v16, v24, v96
	s_waitcnt vmcnt(1)
	v_fmac_f32_e32 v14, v15, v98
	v_fma_f32 v15, v17, -2.0, 1.0
	v_mul_f32_e32 v16, 0x4038aa3b, v16
	v_add_f32_e32 v17, v25, v97
	v_exp_f32_e32 v16, v16
	v_mul_f32_e32 v17, 0x4038aa3b, v17
	v_add_f32_e32 v6, v26, v6
	v_exp_f32_e32 v17, v17
	v_mul_f32_e32 v6, 0x4038aa3b, v6
	v_exp_f32_e32 v6, v6
	v_fmac_f32_e32 v14, v15, v99
	v_add_f32_e32 v15, 1.0, v16
	v_rcp_f32_e32 v15, v15
	v_add_f32_e32 v16, 1.0, v17
	v_rcp_f32_e32 v16, v16
	v_add_f32_e32 v6, 1.0, v6
	v_rcp_f32_e32 v6, v6
	v_add_f32_e32 v7, v27, v7
	v_mul_f32_e32 v7, 0x4038aa3b, v7
	v_fma_f32 v15, v15, -2.0, 1.0
	v_exp_f32_e32 v7, v7
	v_fmac_f32_e32 v14, v15, v100
	v_fma_f32 v15, v16, -2.0, 1.0
	v_fmac_f32_e32 v14, v15, v101
	v_fma_f32 v6, v6, -2.0, 1.0
	s_waitcnt vmcnt(0)
	v_fmac_f32_e32 v14, v6, v2
	v_add_f32_e32 v6, v28, v8
	v_add_f32_e32 v2, 1.0, v7
	v_mul_f32_e32 v6, 0x4038aa3b, v6
	v_add_f32_e32 v7, v29, v9
	v_exp_f32_e32 v6, v6
	v_mul_f32_e32 v7, 0x4038aa3b, v7
	v_exp_f32_e32 v7, v7
	v_rcp_f32_e32 v2, v2
	v_add_f32_e32 v6, 1.0, v6
	v_rcp_f32_e32 v6, v6
	v_add_f32_e32 v7, 1.0, v7
	v_rcp_f32_e32 v7, v7
	v_fma_f32 v2, v2, -2.0, 1.0
	v_fmac_f32_e32 v14, v2, v3
	v_fma_f32 v2, v6, -2.0, 1.0
	v_fmac_f32_e32 v14, v2, v4
	v_fma_f32 v2, v7, -2.0, 1.0
	v_fmac_f32_e32 v14, v2, v5
	v_mov_b32_e32 v2, v14
	s_nop 1
	v_permlane16_swap_b32_e32 v14, v2
	v_add_f32_e32 v2, v14, v2
	v_mov_b32_e32 v3, v2
	s_nop 1
	v_permlane32_swap_b32_e32 v2, v3
	v_add_f32_e32 v2, v2, v3
	s_and_saveexec_b64 s[4:5], s[8:9]
	v_lshl_or_b32 v3, v11, 6, v0
	v_add_u32_e32 v3, 0x10000, v3
	ds_write_b32 v3, v2
	s_or_b64 exec, exec, s[4:5]
	v_cmp_eq_u32_e64 s[4:5], 0, v12
	s_and_b64 s[2:3], s[4:5], s[2:3]
	s_and_b64 s[2:3], s[2:3], vcc
	s_waitcnt lgkmcnt(0)
	s_barrier
	s_and_saveexec_b64 s[4:5], s[2:3]
	s_cbranch_execz .LBB1_4
	v_lshl_or_b32 v0, v11, 6, v0
	v_add_u32_e32 v0, 0x10000, v0
	ds_read_b32 v0, v0
	s_load_dwordx2 s[0:1], s[0:1], 0x30
	s_movk_i32 s2, 0xc8
	s_waitcnt lgkmcnt(0)
	v_add_f32_e32 v0, v2, v0
	v_add_f32_e32 v0, s6, v0
	v_mul_f32_e32 v0, 0xbfb8aa3b, v0
	v_exp_f32_e32 v0, v0
	s_nop 0
	v_add_f32_e32 v0, 1.0, v0
	v_rcp_f32_e32 v2, v0
	v_mad_u64_u32 v[0:1], s[2:3], v1, s2, v[10:11]
	v_ashrrev_i32_e32 v1, 31, v0
	v_lshl_add_u64 v[0:1], v[0:1], 2, s[0:1]
	global_store_dword v[0:1], v2, off
